# P8: next-unit gather index loads issued at unit start, no vmcnt(0) drain inside the K loop
# baseline (speedup 1.0000x reference)
.LBB0_1346:
	s_ashr_i32 s17, s16, 31
	s_lshl_b64 s[24:25], s[16:17], 16
	s_add_i32 s17, s50, 0x80
	v_add_u32_e32 v202, s17, v1
	v_add_u32_e32 v203, s17, v190
	s_lshl_b32 s17, s16, 2
	s_add_i32 s17, s17, 0
	s_add_i32 s17, s17, 0x20000
	s_add_u32 s24, s18, s24
	s_addc_u32 s25, s19, s25
	v_mov_b32_e32 v175, v167
	v_mov_b32_e32 v173, v167
	s_add_u32 s56, s26, 0x100
	v_mov_b32_e32 v58, 0
	v_add_u32_e32 v200, s50, v1
	v_add_u32_e32 v201, s50, v190
	v_lshl_add_u64 v[178:179], s[10:11], 0, v[172:173]
	v_lshl_add_u64 v[180:181], s[10:11], 0, v[174:175]
	s_addc_u32 s57, s27, 0
	s_mov_b32 s58, -2
	s_mov_b64 s[26:27], 0
	s_xor_b64 s[28:29], s[22:23], -1
	v_mov_b32_e32 v169, v199
	v_mov_b32_e32 v171, v176
	v_mov_b32_e32 v173, v174
	v_mov_b32_e32 v175, v172
	s_and_b64 vcc, exec, s[28:29]
	s_cbranch_vccnz .Lmy_gu_noidx
	v_mov_b32_e32 v2, s17
	ds_read_b32 v2, v2
	s_waitcnt lgkmcnt(0)
	v_readfirstlane_b32 s30, v2
	s_nop 1
	v_cmp_gt_i32_e32 vcc, s30, v200
	s_nop 1
	v_cndmask_b32_e32 v2, 0, v200, vcc
	v_cmp_gt_i32_e32 vcc, s30, v201
	v_ashrrev_i32_e32 v3, 31, v2
	v_lshl_add_u64 v[2:3], v[2:3], 2, s[24:25]
	v_cndmask_b32_e32 v4, 0, v201, vcc
	v_cmp_gt_i32_e32 vcc, s30, v202
	v_ashrrev_i32_e32 v5, 31, v4
	v_lshl_add_u64 v[4:5], v[4:5], 2, s[24:25]
	v_cndmask_b32_e32 v6, 0, v202, vcc
	v_cmp_gt_i32_e32 vcc, s30, v203
	v_ashrrev_i32_e32 v7, 31, v6
	v_lshl_add_u64 v[6:7], v[6:7], 2, s[24:25]
	v_cndmask_b32_e32 v8, 0, v203, vcc
	v_ashrrev_i32_e32 v9, 31, v8
	v_lshl_add_u64 v[8:9], v[8:9], 2, s[24:25]
	global_load_dword v241, v[2:3], off
	s_nop 0
	global_load_dword v242, v[4:5], off
	s_nop 0
	global_load_dword v243, v[6:7], off
	global_load_dword v244, v[8:9], off
.Lmy_gu_noidx:
	v_mov_b32_e32 v59, v58
	v_mov_b32_e32 v60, v58
	v_mov_b32_e32 v61, v58
	v_mov_b32_e32 v74, v58
	v_mov_b32_e32 v75, v58
	v_mov_b32_e32 v76, v58
	v_mov_b32_e32 v77, v58
	v_mov_b32_e32 v82, v58
	v_mov_b32_e32 v83, v58
	v_mov_b32_e32 v84, v58
	v_mov_b32_e32 v85, v58
	v_mov_b32_e32 v90, v58
	v_mov_b32_e32 v91, v58
	v_mov_b32_e32 v92, v58
	v_mov_b32_e32 v93, v58
	v_mov_b32_e32 v34, v58
	v_mov_b32_e32 v35, v58
	v_mov_b32_e32 v36, v58
	v_mov_b32_e32 v37, v58
	v_mov_b32_e32 v38, v58
	v_mov_b32_e32 v39, v58
	v_mov_b32_e32 v40, v58
	v_mov_b32_e32 v41, v58
	v_mov_b32_e32 v46, v58
	v_mov_b32_e32 v47, v58
	v_mov_b32_e32 v48, v58
	v_mov_b32_e32 v49, v58
	v_mov_b32_e32 v54, v58
	v_mov_b32_e32 v55, v58
	v_mov_b32_e32 v56, v58
	v_mov_b32_e32 v57, v58
	v_mov_b32_e32 v66, v58
	v_mov_b32_e32 v67, v58
	v_mov_b32_e32 v68, v58
	v_mov_b32_e32 v69, v58
	v_mov_b32_e32 v78, v58
	v_mov_b32_e32 v79, v58
	v_mov_b32_e32 v80, v58
	v_mov_b32_e32 v81, v58
	v_mov_b32_e32 v86, v58
	v_mov_b32_e32 v87, v58
	v_mov_b32_e32 v88, v58
	v_mov_b32_e32 v89, v58
	v_mov_b32_e32 v94, v58
	v_mov_b32_e32 v95, v58
	v_mov_b32_e32 v96, v58
	v_mov_b32_e32 v97, v58
	v_mov_b32_e32 v98, v58
	v_mov_b32_e32 v99, v58
	v_mov_b32_e32 v100, v58
	v_mov_b32_e32 v101, v58
	v_mov_b32_e32 v106, v58
	v_mov_b32_e32 v107, v58
	v_mov_b32_e32 v108, v58
	v_mov_b32_e32 v109, v58
	v_mov_b32_e32 v114, v58
	v_mov_b32_e32 v115, v58
	v_mov_b32_e32 v116, v58
	v_mov_b32_e32 v117, v58
	v_mov_b32_e32 v122, v58
	v_mov_b32_e32 v123, v58
	v_mov_b32_e32 v124, v58
	v_mov_b32_e32 v125, v58
	v_mov_b32_e32 v130, v58
	v_mov_b32_e32 v131, v58
	v_mov_b32_e32 v132, v58
	v_mov_b32_e32 v133, v58
	v_mov_b32_e32 v138, v58
	v_mov_b32_e32 v139, v58
	v_mov_b32_e32 v140, v58
	v_mov_b32_e32 v141, v58
	v_mov_b32_e32 v146, v58
	v_mov_b32_e32 v147, v58
	v_mov_b32_e32 v148, v58
	v_mov_b32_e32 v149, v58
	v_mov_b32_e32 v154, v58
	v_mov_b32_e32 v155, v58
	v_mov_b32_e32 v156, v58
	v_mov_b32_e32 v157, v58
	v_mov_b32_e32 v102, v58
	v_mov_b32_e32 v103, v58
	v_mov_b32_e32 v104, v58
	v_mov_b32_e32 v105, v58
	v_mov_b32_e32 v110, v58
	v_mov_b32_e32 v111, v58
	v_mov_b32_e32 v112, v58
	v_mov_b32_e32 v113, v58
	v_mov_b32_e32 v118, v58
	v_mov_b32_e32 v119, v58
	v_mov_b32_e32 v120, v58
	v_mov_b32_e32 v121, v58
	v_mov_b32_e32 v126, v58
	v_mov_b32_e32 v127, v58
	v_mov_b32_e32 v128, v58
	v_mov_b32_e32 v129, v58
	v_mov_b32_e32 v134, v58
	v_mov_b32_e32 v135, v58
	v_mov_b32_e32 v136, v58
	v_mov_b32_e32 v137, v58
	v_mov_b32_e32 v142, v58
	v_mov_b32_e32 v143, v58
	v_mov_b32_e32 v144, v58
	v_mov_b32_e32 v145, v58
	v_mov_b32_e32 v150, v58
	v_mov_b32_e32 v151, v58
	v_mov_b32_e32 v152, v58
	v_mov_b32_e32 v153, v58
	v_mov_b32_e32 v158, v58
	v_mov_b32_e32 v159, v58
	v_mov_b32_e32 v160, v58
	v_mov_b32_e32 v161, v58
	v_mov_b32_e32 v70, v58
	v_mov_b32_e32 v71, v58
	v_mov_b32_e32 v72, v58
	v_mov_b32_e32 v73, v58
	v_mov_b32_e32 v62, v58
	v_mov_b32_e32 v63, v58
	v_mov_b32_e32 v64, v58
	v_mov_b32_e32 v65, v58
	v_mov_b32_e32 v50, v58
	v_mov_b32_e32 v51, v58
	v_mov_b32_e32 v52, v58
	v_mov_b32_e32 v53, v58
	v_mov_b32_e32 v42, v58
	v_mov_b32_e32 v43, v58
	v_mov_b32_e32 v44, v58
	v_mov_b32_e32 v45, v58
	s_branch .LBB0_1348

.LBB0_1348:
	s_cmpk_lg_i32 s26, 0x600
	s_cselect_b64 s[30:31], -1, 0
	s_or_b64 s[30:31], s[28:29], s[30:31]
	s_and_b64 vcc, exec, s[30:31]
	s_cbranch_vccnz .LBB0_1347
	s_waitcnt vmcnt(8)
	v_lshl_add_u32 v169, v241, 11, v191
	v_lshl_add_u32 v171, v242, 11, v192
	v_lshl_add_u32 v173, v243, 11, v191
	v_lshl_add_u32 v175, v244, 11, v192
	s_branch .LBB0_1347
